# baseline (speedup 1.0000x reference)
.Lmynosl:
	v_sub_u32_e64 v115, v117, 2 clamp
	v_lshlrev_b32_e32 v115, 11, v115
	v_add_u32_e32 v116, v115, v112
	v_add_u32_e64 v115, v115, v113
	buffer_load_dwordx2 v[0:1], v116, s[4:7], 0 offen nt
	buffer_load_dwordx2 v[6:7], v116, s[4:7], 0 offen nt
	buffer_load_dwordx4 v[2:5], v115, s[4:7], 0 offen nt
	v_sub_u32_e64 v115, v117, 1 clamp
	v_lshlrev_b32_e32 v115, 11, v115
	v_add_u32_e32 v116, v115, v112
	v_add_u32_e64 v115, v115, v113
	buffer_load_dwordx2 v[8:9], v116, s[4:7], 0 offen nt
	buffer_load_dwordx2 v[14:15], v116, s[4:7], 0 offen nt
	buffer_load_dwordx4 v[10:13], v115, s[4:7], 0 offen nt
	v_lshlrev_b32_e32 v115, 11, v117
	v_add_u32_e32 v124, v115, v112
	v_add_u32_e32 v125, v115, v113
	v_mov_b32_e32 v114, v125
	v_add_u32_e32 v119, 0x1000, v114
	buffer_load_dwordx2 v[16:17], v124, s[4:7], 0 offen nt
	buffer_load_dwordx2 v[22:23], v124, s[4:7], 0 offen nt
	buffer_load_dwordx4 v[18:21], v125, s[4:7], 0 offen nt
	buffer_load_dwordx2 v[24:25], v124, s[4:7], 0 offen offset:2048 nt
	buffer_load_dwordx2 v[30:31], v124, s[4:7], 0 offen offset:2048 nt
	buffer_load_dwordx4 v[26:29], v125, s[4:7], 0 offen offset:2048 nt
	v_lshlrev_b32_e64 v115, 11, v117
	v_add_u32_e32 v115, 0x1000, v115
	v_add_u32_e32 v124, v115, v112
	v_add_u32_e32 v125, v115, v113
	buffer_load_dwordx2 v[32:33], v124, s[4:7], 0 offen nt
	buffer_load_dwordx2 v[38:39], v124, s[4:7], 0 offen nt
	buffer_load_dwordx4 v[34:37], v125, s[4:7], 0 offen nt
	buffer_load_dwordx2 v[40:41], v124, s[4:7], 0 offen offset:2048 nt
	buffer_load_dwordx2 v[46:47], v124, s[4:7], 0 offen offset:2048 nt
	buffer_load_dwordx4 v[42:45], v125, s[4:7], 0 offen offset:2048 nt
	v_min_u32_e32 v115, 0x1fb, v117
	v_lshlrev_b32_e64 v115, 11, v115
	v_add_u32_e32 v115, 0x2000, v115
	v_add_u32_e32 v116, v115, v112
	v_add_u32_e32 v115, v115, v113
	buffer_load_dwordx2 v[48:49], v116, s[4:7], 0 offen nt
	buffer_load_dwordx2 v[54:55], v116, s[4:7], 0 offen nt
	buffer_load_dwordx4 v[50:53], v115, s[4:7], 0 offen nt
	v_min_u32_e32 v115, 0x1fa, v117
	v_lshlrev_b32_e64 v115, 11, v115
	v_add_u32_e32 v115, 0x2800, v115
	v_add_u32_e32 v116, v115, v112
	v_add_u32_e32 v115, v115, v113
	buffer_load_dwordx2 v[56:57], v116, s[4:7], 0 offen nt
	buffer_load_dwordx2 v[62:63], v116, s[4:7], 0 offen nt
	buffer_load_dwordx4 v[58:61], v115, s[4:7], 0 offen nt
	s_cmp_eq_u32 s19, 0
	s_cbranch_scc1 .Lmyp0
	s_cmp_eq_u32 s19, 1
	s_cbranch_scc1 .Lmyp1
	s_setprio 0
	s_branch .Lmypd
